# MoE GEMMs (P10/P11): XCD-aware slot permutation, each XCD covers 8 row tiles x 4 column tiles per round
# baseline (speedup 1.0000x reference)
;     __device__ bool next(int i, Unit& u) const {
;         const int L = i * G + c; if (L >= ntiles * nN) return false;
;         const int ti = L / nN, pn = L % nN;
;         const int e = __builtin_amdgcn_readfirstlane(tile_e[ti]);
;         u.row0 = ti * BM; u.col0 = pn * BM; u.e = e; u.A = A + (size_t)ti * atile; u.B = B + (size_t)e * bexp + (size_t)pn * btile; return true;
; __global__ void __launch_bounds__(512, 2) mega_fwd(Args args) {
;     ...
;         pg8::Gemm g{DM, DM, DM, 0x7f7f7f7f, 0x79797979, LIST, tab}; pg8::GroupedOrder S; S.tile_e = tab + MOE_TILE_E; S.ntiles = __builtin_amdgcn_readfirstlane(tab[64]); S.nN = 16; S.G = G; S.c = bx;
.LBB0_2355:
	s_or_b64 exec, exec, s[4:5]
	s_add_i32 s3, 0, 0x25900
	v_mov_b32_e32 v1, s3
	s_waitcnt lgkmcnt(0)
	s_barrier
	ds_read_b32 v1, v1
	s_waitcnt lgkmcnt(0)
	v_readfirstlane_b32 s3, v1
	s_lshl_b32 s39, s3, 4
	s_mov_b32 s100, s2
	s_cmp_lg_u32 s82, 0x100
	s_cbranch_scc1 .Lp10_noperm
	s_and_b32 s98, s2, 7
	s_lshr_b32 s99, s2, 3
	s_lshr_b32 s100, s98, 2
	s_lshl_b32 s100, s100, 7
	s_and_b32 s98, s98, 3
	s_lshl_b32 s98, s98, 2
	s_add_i32 s100, s100, s98
	s_and_b32 s98, s99, 3
	s_add_i32 s100, s100, s98
	s_lshr_b32 s99, s99, 2
	s_lshl_b32 s99, s99, 4
	s_add_i32 s100, s100, s99
.Lp10_noperm:
	s_cmp_lt_i32 s100, s39
	s_cselect_b64 s[4:5], -1, 0
	s_cmp_ge_i32 s100, s39
	v_readfirstlane_b32 s3, v0
	s_cbranch_scc1 .LBB0_2357
	s_ashr_i32 s12, s100, 31
	s_lshr_b32 s12, s12, 28
	s_add_i32 s12, s100, s12
	s_ashr_i32 s13, s12, 4
	s_lshl_b32 s16, s13, 2
	s_add_i32 s16, s16, 0
	s_add_i32 s16, s16, 0x25a04
	v_mov_b32_e32 v1, s16
	ds_read_b32 v1, v1
	s_and_b32 s12, s12, -16
	s_sub_i32 s16, s100, s12
	s_lshl_b32 s41, s13, 8
	s_lshl_b32 s72, s16, 8
	s_waitcnt lgkmcnt(0)
	v_readfirstlane_b32 s12, v1
	s_ashr_i32 s13, s12, 31
	s_lshl_b64 s[26:27], s[12:13], 23
	s_add_u32 s13, s80, s26
	s_addc_u32 s22, s81, s27
	s_ashr_i32 s17, s16, 31
	s_lshl_b64 s[16:17], s[16:17], 19
	s_add_u32 s16, s13, s16
	s_addc_u32 s17, s22, s17
	s_mov_b64 s[34:35], s[24:25]
	s_andn2_b64 vcc, exec, s[4:5]
	s_cbranch_vccz .LBB0_2358
	s_branch .LBB0_2481

;     __device__ bool next(int i, Unit& u) const {
;         const int L = i * G + c; if (L >= ntiles * nN) return false;
;         const int ti = L / nN, pn = L % nN;
;         const int e = __builtin_amdgcn_readfirstlane(tile_e[ti]);
; template <class Epi, class Sched, bool F8 = false, bool MID = false, bool GATHER = false>
; __device__ __forceinline__ void gemm_phase(LAS unsigned char* lds, const Gemm g, const Sched& S, const Epi& E) {
;     ...
;     if constexpr (GATHER) { Unit uu;
;         for (int i = 0; i < 20 && S.next(i, uu); ++i) if (tid < 256) { const int l_ = uu.row0 - g.tab[uu.e] + tid; rt[i * 256 + tid] = l_ < g.tab[32 + uu.e] ? g.list[uu.e * T + l_] : T; }
.LBB0_2358:
	s_mov_b32 s101, 0
	s_load_dwordx2 s[50:51], s[0:1], 0x80
	s_load_dwordx2 s[52:53], s[0:1], 0x90
	s_mov_b32 s13, 0x20000
	v_mbcnt_lo_u32_b32 v1, -1, 0
	v_mbcnt_hi_u32_b32 v1, -1, v1
	v_mul_lo_u32 v2, v1, s82
	v_add_u32_e32 v2, s100, v2
	v_cmp_gt_i32_e32 vcc, s39, v2
	v_lshrrev_b32_e32 v3, 4, v2
	v_min_u32_e32 v4, 0x13f, v3
	v_lshlrev_b32_e32 v4, 2, v4
	v_add_u32_e32 v4, 0x25a04, v4
	ds_read_b32 v5, v4
	s_mov_b64 s[54:55], vcc
	s_waitcnt lgkmcnt(0)
	v_lshlrev_b32_e32 v6, 2, v5
	v_add_u32_e32 v6, 0x25800, v6
	ds_read2_b32 v[6:7], v6 offset1:32
	v_lshlrev_b32_e32 v3, 8, v3
	v_cmp_gt_u32_e32 vcc, 0x100, v0
	v_lshl_add_u32 v1, v0, 2, s13
	s_mov_b64 s[56:57], vcc
	s_waitcnt lgkmcnt(0)
	v_sub_u32_e32 v3, v3, v6
	s_bitcmp1_b32 s54, 0
	s_cbranch_scc0 .Lrt_issued
	v_readlane_b32 s4, v5, 0
	v_readlane_b32 s5, v3, 0
	v_readlane_b32 s22, v7, 0
	v_mov_b32_e32 v200, 0x4000
	s_nop 1
	v_add_u32_e32 v8, s5, v0
	v_cmp_gt_i32_e32 vcc, s22, v8
	s_lshl_b32 s4, s4, 14
	s_nop 0
	s_and_b64 vcc, vcc, s[56:57]
	v_add_lshl_u32 v8, v8, s4, 2
	s_and_saveexec_b64 s[26:27], vcc
	global_load_dword v200, v8, s[48:49]
	s_mov_b64 exec, s[26:27]
	s_bitcmp1_b32 s54, 1
	s_cbranch_scc0 .Lrt_issued
	v_readlane_b32 s4, v5, 1
	v_readlane_b32 s5, v3, 1
	v_readlane_b32 s22, v7, 1
	v_mov_b32_e32 v201, 0x4000
	s_nop 1
	v_add_u32_e32 v8, s5, v0
	v_cmp_gt_i32_e32 vcc, s22, v8
	s_lshl_b32 s4, s4, 14
	s_nop 0
	s_and_b64 vcc, vcc, s[56:57]
	v_add_lshl_u32 v8, v8, s4, 2
	s_and_saveexec_b64 s[26:27], vcc
	global_load_dword v201, v8, s[48:49]
	s_mov_b64 exec, s[26:27]
	s_bitcmp1_b32 s54, 2
	s_cbranch_scc0 .Lrt_issued
	v_readlane_b32 s4, v5, 2
	v_readlane_b32 s5, v3, 2
	v_readlane_b32 s22, v7, 2
	v_mov_b32_e32 v202, 0x4000
	s_nop 1
	v_add_u32_e32 v8, s5, v0
	v_cmp_gt_i32_e32 vcc, s22, v8
	s_lshl_b32 s4, s4, 14
	s_nop 0
	s_and_b64 vcc, vcc, s[56:57]
	v_add_lshl_u32 v8, v8, s4, 2
	s_and_saveexec_b64 s[26:27], vcc
	global_load_dword v202, v8, s[48:49]
	s_mov_b64 exec, s[26:27]
	s_bitcmp1_b32 s54, 3
	s_cbranch_scc0 .Lrt_issued
	v_readlane_b32 s4, v5, 3
	v_readlane_b32 s5, v3, 3
	v_readlane_b32 s22, v7, 3
	v_mov_b32_e32 v203, 0x4000
	s_nop 1
	v_add_u32_e32 v8, s5, v0
	v_cmp_gt_i32_e32 vcc, s22, v8
	s_lshl_b32 s4, s4, 14
	s_nop 0
	s_and_b64 vcc, vcc, s[56:57]
	v_add_lshl_u32 v8, v8, s4, 2
	s_and_saveexec_b64 s[26:27], vcc
	global_load_dword v203, v8, s[48:49]
	s_mov_b64 exec, s[26:27]
	s_bitcmp1_b32 s54, 4
	s_cbranch_scc0 .Lrt_issued
	v_readlane_b32 s4, v5, 4
	v_readlane_b32 s5, v3, 4
	v_readlane_b32 s22, v7, 4
	v_mov_b32_e32 v204, 0x4000
	s_nop 1
	v_add_u32_e32 v8, s5, v0
	v_cmp_gt_i32_e32 vcc, s22, v8
	s_lshl_b32 s4, s4, 14
	s_nop 0
	s_and_b64 vcc, vcc, s[56:57]
	v_add_lshl_u32 v8, v8, s4, 2
	s_and_saveexec_b64 s[26:27], vcc
	global_load_dword v204, v8, s[48:49]
	s_mov_b64 exec, s[26:27]
	s_bitcmp1_b32 s54, 5
	s_cbranch_scc0 .Lrt_issued
	v_readlane_b32 s4, v5, 5
	v_readlane_b32 s5, v3, 5
	v_readlane_b32 s22, v7, 5
	v_mov_b32_e32 v205, 0x4000
	s_nop 1
	v_add_u32_e32 v8, s5, v0
	v_cmp_gt_i32_e32 vcc, s22, v8
	s_lshl_b32 s4, s4, 14
	s_nop 0
	s_and_b64 vcc, vcc, s[56:57]
	v_add_lshl_u32 v8, v8, s4, 2
	s_and_saveexec_b64 s[26:27], vcc
	global_load_dword v205, v8, s[48:49]
	s_mov_b64 exec, s[26:27]
	s_bitcmp1_b32 s54, 6
	s_cbranch_scc0 .Lrt_issued
	v_readlane_b32 s4, v5, 6
	v_readlane_b32 s5, v3, 6
	v_readlane_b32 s22, v7, 6
	v_mov_b32_e32 v206, 0x4000
	s_nop 1
	v_add_u32_e32 v8, s5, v0
	v_cmp_gt_i32_e32 vcc, s22, v8
	s_lshl_b32 s4, s4, 14
	s_nop 0
	s_and_b64 vcc, vcc, s[56:57]
	v_add_lshl_u32 v8, v8, s4, 2
	s_and_saveexec_b64 s[26:27], vcc
	global_load_dword v206, v8, s[48:49]
	s_mov_b64 exec, s[26:27]
	s_bitcmp1_b32 s54, 7
	s_cbranch_scc0 .Lrt_issued
	v_readlane_b32 s4, v5, 7
	v_readlane_b32 s5, v3, 7
	v_readlane_b32 s22, v7, 7
	v_mov_b32_e32 v207, 0x4000
	s_nop 1
	v_add_u32_e32 v8, s5, v0
	v_cmp_gt_i32_e32 vcc, s22, v8
	s_lshl_b32 s4, s4, 14
	s_nop 0
	s_and_b64 vcc, vcc, s[56:57]
	v_add_lshl_u32 v8, v8, s4, 2
	s_and_saveexec_b64 s[26:27], vcc
	global_load_dword v207, v8, s[48:49]
	s_mov_b64 exec, s[26:27]
	s_bitcmp1_b32 s54, 8
	s_cbranch_scc0 .Lrt_issued
	v_readlane_b32 s4, v5, 8
	v_readlane_b32 s5, v3, 8
	v_readlane_b32 s22, v7, 8
	v_mov_b32_e32 v208, 0x4000
	s_nop 1
	v_add_u32_e32 v8, s5, v0
	v_cmp_gt_i32_e32 vcc, s22, v8
	s_lshl_b32 s4, s4, 14
	s_nop 0
	s_and_b64 vcc, vcc, s[56:57]
	v_add_lshl_u32 v8, v8, s4, 2
	s_and_saveexec_b64 s[26:27], vcc
	global_load_dword v208, v8, s[48:49]
	s_mov_b64 exec, s[26:27]
	s_bitcmp1_b32 s54, 9
	s_cbranch_scc0 .Lrt_issued
; template <class Epi, class Sched, bool F8 = false, bool MID = false, bool GATHER = false>
; __device__ __forceinline__ void gemm_phase(LAS unsigned char* lds, const Gemm g, const Sched& S, const Epi& E) {
;     ...
;         for (int i = 0; i < 20 && S.next(i, uu); ++i) if (tid < 256) { const int l_ = uu.row0 - g.tab[uu.e] + tid; rt[i * 256 + tid] = l_ < g.tab[32 + uu.e] ? g.list[uu.e * T + l_] : T; }
	v_readlane_b32 s4, v5, 9
	v_readlane_b32 s5, v3, 9
	v_readlane_b32 s22, v7, 9
	v_mov_b32_e32 v209, 0x4000
	s_nop 1
	v_add_u32_e32 v8, s5, v0
	v_cmp_gt_i32_e32 vcc, s22, v8
	s_lshl_b32 s4, s4, 14
	s_nop 0
	s_and_b64 vcc, vcc, s[56:57]
	v_add_lshl_u32 v8, v8, s4, 2
	s_and_saveexec_b64 s[26:27], vcc
	global_load_dword v209, v8, s[48:49]
	s_mov_b64 exec, s[26:27]
	s_bitcmp1_b32 s54, 10
	s_cbranch_scc0 .Lrt_issued
	v_readlane_b32 s4, v5, 10
	v_readlane_b32 s5, v3, 10
	v_readlane_b32 s22, v7, 10
	v_mov_b32_e32 v210, 0x4000
	s_nop 1
	v_add_u32_e32 v8, s5, v0
	v_cmp_gt_i32_e32 vcc, s22, v8
	s_lshl_b32 s4, s4, 14
	s_nop 0
	s_and_b64 vcc, vcc, s[56:57]
	v_add_lshl_u32 v8, v8, s4, 2
	s_and_saveexec_b64 s[26:27], vcc
	global_load_dword v210, v8, s[48:49]
	s_mov_b64 exec, s[26:27]
	s_bitcmp1_b32 s54, 11
	s_cbranch_scc0 .Lrt_issued
	v_readlane_b32 s4, v5, 11
	v_readlane_b32 s5, v3, 11
	v_readlane_b32 s22, v7, 11
	v_mov_b32_e32 v211, 0x4000
	s_nop 1
	v_add_u32_e32 v8, s5, v0
	v_cmp_gt_i32_e32 vcc, s22, v8
	s_lshl_b32 s4, s4, 14
	s_nop 0
	s_and_b64 vcc, vcc, s[56:57]
	v_add_lshl_u32 v8, v8, s4, 2
	s_and_saveexec_b64 s[26:27], vcc
	global_load_dword v211, v8, s[48:49]
	s_mov_b64 exec, s[26:27]
	s_bitcmp1_b32 s54, 12
	s_cbranch_scc0 .Lrt_issued
	v_readlane_b32 s4, v5, 12
	v_readlane_b32 s5, v3, 12
	v_readlane_b32 s22, v7, 12
	v_mov_b32_e32 v212, 0x4000
	s_nop 1
	v_add_u32_e32 v8, s5, v0
	v_cmp_gt_i32_e32 vcc, s22, v8
	s_lshl_b32 s4, s4, 14
	s_nop 0
	s_and_b64 vcc, vcc, s[56:57]
	v_add_lshl_u32 v8, v8, s4, 2
	s_and_saveexec_b64 s[26:27], vcc
	global_load_dword v212, v8, s[48:49]
	s_mov_b64 exec, s[26:27]
	s_bitcmp1_b32 s54, 13
	s_cbranch_scc0 .Lrt_issued
	v_readlane_b32 s4, v5, 13
	v_readlane_b32 s5, v3, 13
	v_readlane_b32 s22, v7, 13
	v_mov_b32_e32 v213, 0x4000
	s_nop 1
	v_add_u32_e32 v8, s5, v0
	v_cmp_gt_i32_e32 vcc, s22, v8
	s_lshl_b32 s4, s4, 14
	s_nop 0
	s_and_b64 vcc, vcc, s[56:57]
	v_add_lshl_u32 v8, v8, s4, 2
	s_and_saveexec_b64 s[26:27], vcc
	global_load_dword v213, v8, s[48:49]
	s_mov_b64 exec, s[26:27]
	s_bitcmp1_b32 s54, 14
	s_cbranch_scc0 .Lrt_issued
	v_readlane_b32 s4, v5, 14
	v_readlane_b32 s5, v3, 14
	v_readlane_b32 s22, v7, 14
	v_mov_b32_e32 v214, 0x4000
	s_nop 1
	v_add_u32_e32 v8, s5, v0
	v_cmp_gt_i32_e32 vcc, s22, v8
	s_lshl_b32 s4, s4, 14
	s_nop 0
	s_and_b64 vcc, vcc, s[56:57]
	v_add_lshl_u32 v8, v8, s4, 2
	s_and_saveexec_b64 s[26:27], vcc
	global_load_dword v214, v8, s[48:49]
	s_mov_b64 exec, s[26:27]
	s_bitcmp1_b32 s54, 15
	s_cbranch_scc0 .Lrt_issued
	v_readlane_b32 s4, v5, 15
	v_readlane_b32 s5, v3, 15
	v_readlane_b32 s22, v7, 15
	v_mov_b32_e32 v215, 0x4000
	s_nop 1
	v_add_u32_e32 v8, s5, v0
	v_cmp_gt_i32_e32 vcc, s22, v8
	s_lshl_b32 s4, s4, 14
	s_nop 0
	s_and_b64 vcc, vcc, s[56:57]
	v_add_lshl_u32 v8, v8, s4, 2
	s_and_saveexec_b64 s[26:27], vcc
	global_load_dword v215, v8, s[48:49]
	s_mov_b64 exec, s[26:27]
	s_bitcmp1_b32 s54, 16
	s_cbranch_scc0 .Lrt_issued
	v_readlane_b32 s4, v5, 16
	v_readlane_b32 s5, v3, 16
	v_readlane_b32 s22, v7, 16
	v_mov_b32_e32 v216, 0x4000
	s_nop 1
	v_add_u32_e32 v8, s5, v0
	v_cmp_gt_i32_e32 vcc, s22, v8
	s_lshl_b32 s4, s4, 14
	s_nop 0
	s_and_b64 vcc, vcc, s[56:57]
	v_add_lshl_u32 v8, v8, s4, 2
	s_and_saveexec_b64 s[26:27], vcc
	global_load_dword v216, v8, s[48:49]
	s_mov_b64 exec, s[26:27]
	s_bitcmp1_b32 s54, 17
	s_cbranch_scc0 .Lrt_issued
	v_readlane_b32 s4, v5, 17
	v_readlane_b32 s5, v3, 17
	v_readlane_b32 s22, v7, 17
	v_mov_b32_e32 v217, 0x4000
	s_nop 1
	v_add_u32_e32 v8, s5, v0
	v_cmp_gt_i32_e32 vcc, s22, v8
	s_lshl_b32 s4, s4, 14
	s_nop 0
	s_and_b64 vcc, vcc, s[56:57]
	v_add_lshl_u32 v8, v8, s4, 2
	s_and_saveexec_b64 s[26:27], vcc
	global_load_dword v217, v8, s[48:49]
	s_mov_b64 exec, s[26:27]
	s_bitcmp1_b32 s54, 18
	s_cbranch_scc0 .Lrt_issued
	v_readlane_b32 s4, v5, 18
	v_readlane_b32 s5, v3, 18
	v_readlane_b32 s22, v7, 18
	v_mov_b32_e32 v218, 0x4000
	s_nop 1
	v_add_u32_e32 v8, s5, v0
	v_cmp_gt_i32_e32 vcc, s22, v8
	s_lshl_b32 s4, s4, 14
	s_nop 0
	s_and_b64 vcc, vcc, s[56:57]
	v_add_lshl_u32 v8, v8, s4, 2
	s_and_saveexec_b64 s[26:27], vcc
	global_load_dword v218, v8, s[48:49]
	s_mov_b64 exec, s[26:27]
	s_bitcmp1_b32 s54, 19
	s_cbranch_scc0 .Lrt_issued
	v_readlane_b32 s4, v5, 19
	v_readlane_b32 s5, v3, 19
	v_readlane_b32 s22, v7, 19
	v_mov_b32_e32 v219, 0x4000
	s_nop 1
	v_add_u32_e32 v8, s5, v0
	v_cmp_gt_i32_e32 vcc, s22, v8
	s_lshl_b32 s4, s4, 14
	s_nop 0
	s_and_b64 vcc, vcc, s[56:57]
	v_add_lshl_u32 v8, v8, s4, 2
	s_and_saveexec_b64 s[26:27], vcc
	global_load_dword v219, v8, s[48:49]
	s_mov_b64 exec, s[26:27]

;     __device__ bool next(int i, Unit& u) const {
;         const int L = i * G + c; if (L >= ntiles * nN) return false;
;         const int ti = L / nN, pn = L % nN;
;         const int e = __builtin_amdgcn_readfirstlane(tile_e[ti]);
;         u.row0 = ti * BM; u.col0 = pn * BM; u.e = e; u.A = A + (size_t)ti * atile; u.B = B + (size_t)e * bexp + (size_t)pn * btile; return true;
; template <class Epi, class Sched, bool F8 = false, bool MID = false, bool GATHER = false>
; __device__ __forceinline__ void gemm_phase(LAS unsigned char* lds, const Gemm g, const Sched& S, const Epi& E) {
;     ...
;         const bool has_next = S.next(ui + 1, nxt);
.LBB0_2463:
	s_add_i32 s27, s77, 1
	s_mul_i32 s4, s27, s82
	s_add_i32 s4, s4, s100
	s_cmp_lt_i32 s4, s39
	s_cselect_b64 s[64:65], -1, 0
	s_cmp_ge_i32 s4, s39
	s_cselect_b64 s[58:59], -1, 0
	s_and_b64 vcc, exec, s[58:59]
	s_mov_b64 s[60:61], s[16:17]
	s_mov_b64 s[62:63], s[34:35]
	s_cbranch_vccnz .LBB0_2465
	s_ashr_i32 s3, s4, 31
	s_lshr_b32 s3, s3, 28
	s_add_i32 s3, s4, s3
	s_ashr_i32 s5, s3, 4
	s_lshl_b32 s13, s5, 2
	s_add_i32 s13, s13, 0
	s_add_i32 s13, s13, 0x25a04
	v_mov_b32_e32 v2, s13
	ds_read_b32 v2, v2
	s_and_b32 s3, s3, -16
	s_sub_i32 s4, s4, s3
	s_lshl_b32 s26, s5, 8
	s_lshl_b32 s3, s4, 8
	s_waitcnt lgkmcnt(0)
	v_readfirstlane_b32 s56, v2
	s_ashr_i32 s57, s56, 31
	s_lshl_b64 s[60:61], s[56:57], 23
	s_add_u32 s13, s80, s60
	s_addc_u32 s22, s81, s61
	s_ashr_i32 s5, s4, 31
	s_lshl_b64 s[4:5], s[4:5], 19
	s_add_u32 s60, s13, s4
	s_addc_u32 s61, s22, s5
	s_mov_b64 s[62:63], s[24:25]

; #define PG8_STAGE(bufoff, gbase, voff) do { _Pragma("unroll") for (int _i = 0; _i < 2; ++_i) \
;         asm volatile("s_mov_b32 m0, %0\n\ts_nop 0\n\tglobal_load_lds_dwordx4 %1, %2" :: "s"(ldsb + (unsigned)(bufoff) + ldsw + _i * 8192u), "v"((voff)[_i]), "s"((const char*)(gbase)) : "m0", "memory"); } while (0)
;     __device__ bool next(int i, Unit& u) const {
;         const int L = i * G + c; if (L >= ntiles * nN) return false;
;         const int ti = L / nN, pn = L % nN;
;         const int e = __builtin_amdgcn_readfirstlane(tile_e[ti]);
;         u.row0 = ti * BM; u.col0 = pn * BM; u.e = e; u.A = A + (size_t)ti * atile; u.B = B + (size_t)e * bexp + (size_t)pn * btile; return true;
; template <class Epi, class Sched, bool F8 = false, bool MID = false, bool GATHER = false>
; __device__ __forceinline__ void gemm_phase(LAS unsigned char* lds, const Gemm g, const Sched& S, const Epi& E) {
;     ...
;     const char* cA = cur.A; const char* cB = cur.B;
;     PG8_STAGE(PG8_SB(0, 0), cB, voffB); PG8_STAGE(PG8_SB(0, 1), cB + hstepB, voffB); PG8_STAGE(PG8_SA(0, 0), cA, voffA); PG8_STAGE(PG8_SA(0, 1), cA, voffA1);
.LBB0_2548:
	s_add_i32 s3, 0, 0x25900
	v_mov_b32_e32 v1, s3
	ds_read_b32 v1, v1
	v_readfirstlane_b32 s34, v0
	s_waitcnt lgkmcnt(0)
	v_readfirstlane_b32 s3, v1
	s_lshl_b32 s3, s3, 3
	s_mov_b32 s100, s2
	s_cmp_lg_u32 s82, 0x100
	s_cbranch_scc1 .Lp11_noperm
	s_and_b32 s98, s2, 7
	s_lshr_b32 s99, s2, 3
	s_lshr_b32 s100, s98, 1
	s_lshl_b32 s100, s100, 6
	s_and_b32 s98, s98, 1
	s_lshl_b32 s98, s98, 2
	s_add_i32 s100, s100, s98
	s_and_b32 s98, s99, 3
	s_add_i32 s100, s100, s98
	s_lshr_b32 s99, s99, 2
	s_lshl_b32 s99, s99, 3
	s_add_i32 s100, s100, s99
.Lp11_noperm:
	s_cmp_ge_i32 s100, s3
	s_cbranch_scc1 .LBB0_2564
	v_lshlrev_b32_e32 v1, 4, v0
	s_waitcnt vmcnt(15)
	v_and_b32_e32 v2, 32, v0
	v_bitop3_b32 v1, v1, v2, 48 bitop3:0x6c
	v_and_or_b32 v2, v0, 64, v1
	v_lshrrev_b32_e32 v1, 1, v0
	v_lshrrev_b32_e32 v4, 5, v0
	v_and_b32_e32 v1, 24, v1
	v_and_b32_e32 v4, 4, v4
	v_bfe_u32 v5, v0, 2, 2
	v_bfe_u32 v3, v0, 2, 4
	v_or3_b32 v4, v4, v5, v1
	v_lshrrev_b32_e32 v1, 3, v0
	v_and_or_b32 v5, v1, 48, v3
	s_waitcnt vmcnt(14)
	v_and_or_b32 v6, v1, 32, v4
	v_lshl_or_b32 v1, v5, 11, v2
	v_bfe_u32 v5, v0, 3, 25
	v_or_b32_e32 v5, 64, v5
	s_movk_i32 s8, 0x70
	v_and_or_b32 v3, v5, s8, v3
	s_movk_i32 s8, 0x60
	v_and_or_b32 v4, v5, s8, v4
	s_ashr_i32 s8, s100, 31
	s_lshr_b32 s8, s8, 29
	s_add_i32 s8, s100, s8
	s_ashr_i32 s12, s8, 3
	s_lshl_b32 s9, s12, 2
	s_add_i32 s9, s9, 0
	s_add_i32 s9, s9, 0x25a04
	v_lshl_or_b32 v163, v6, 11, v2
	v_lshl_or_b32 v165, v3, 11, v2
	v_lshl_or_b32 v168, v4, 11, v2
	v_mov_b32_e32 v2, s9
	ds_read_b32 v2, v2
	s_lshr_b32 s48, s34, 6
	s_and_b32 s8, s8, -8
	s_ashr_i32 s13, s12, 31
	s_lshr_b32 s35, s34, 8
	s_lshl_b32 s22, s48, 10
	s_sub_i32 s16, s100, s8
	s_lshl_b64 s[8:9], s[12:13], 19
	s_waitcnt lgkmcnt(0)
	v_readfirstlane_b32 s62, v2
	s_add_u32 s66, s30, s8
	s_addc_u32 s67, s31, s9
	s_ashr_i32 s63, s62, 31
	s_lshl_b64 s[8:9], s[62:63], 22
	v_readlane_b32 s13, v252, 3
	s_add_u32 s13, s13, s8
	s_addc_u32 s23, s84, s9
	s_ashr_i32 s17, s16, 31
	s_lshl_b64 s[8:9], s[16:17], 19
	s_add_u32 s64, s13, s8
	s_addc_u32 s65, s23, s9
	s_add_i32 s17, s22, 0
	s_add_i32 s26, s17, 0x10000
	s_mov_b32 m0, s26
	s_nop 0
	global_load_lds_dwordx4 v163, s[64:65]
	s_add_i32 s27, s17, 0x12000
	s_add_i32 s39, s17, 0x14000
	s_mov_b32 m0, s27
	s_nop 0
	global_load_lds_dwordx4 v168, s[64:65]
	s_add_u32 s8, s64, 0x40000
	s_addc_u32 s9, s65, 0
	s_mov_b32 m0, s39
	s_nop 0
	global_load_lds_dwordx4 v163, s[8:9]
	s_add_i32 s41, s17, 0x16000
	s_mov_b32 m0, s41
	s_nop 0
	global_load_lds_dwordx4 v168, s[8:9]
	s_load_dwordx2 s[4:5], s[0:1], 0xa0
	s_mov_b32 m0, s17
	s_nop 0
	global_load_lds_dwordx4 v1, s[66:67]
	s_add_i32 s74, s17, 0x2000
	s_mov_b32 m0, s74
	s_nop 0
	global_load_lds_dwordx4 v165, s[66:67]
	v_or_b32_e32 v162, 0x40000, v1
	s_add_i32 s75, s17, 0x4000
	s_mov_b32 m0, s75
	s_nop 0
	global_load_lds_dwordx4 v162, s[66:67]
	v_or_b32_e32 v167, 0x40000, v165
	s_add_i32 s76, s17, 0x6000
	s_mov_b32 m0, s76
	s_nop 0
	global_load_lds_dwordx4 v167, s[66:67]
	s_cmp_eq_u32 s35, 1
	s_cselect_b64 s[8:9], -1, 0
	s_cmp_lg_u32 s35, 1
	s_cbranch_scc1 .LBB0_2551
	s_barrier

;     __device__ bool next(int i, Unit& u) const {
;         const int L = i * G + c; if (L >= ntiles * nN) return false;
;         const int ti = L / nN, pn = L % nN;
;         const int e = __builtin_amdgcn_readfirstlane(tile_e[ti]);
;         u.row0 = ti * BM; u.col0 = pn * BM; u.e = e; u.A = A + (size_t)ti * atile; u.B = B + (size_t)e * bexp + (size_t)pn * btile; return true;
; template <class Epi, class Sched, bool F8 = false, bool MID = false, bool GATHER = false>
; __device__ __forceinline__ void gemm_phase(LAS unsigned char* lds, const Gemm g, const Sched& S, const Epi& E) {
;     ...
;         const bool has_next = S.next(ui + 1, nxt);
.LBB0_2554:
	s_add_i32 s79, s79, 1
	s_mul_i32 s55, s79, s82
	s_add_i32 s55, s55, s100
	s_cmp_lt_i32 s55, s3
	s_cselect_b64 s[60:61], -1, 0
	s_cmp_ge_i32 s55, s3
	s_cbranch_scc1 .LBB0_2556
	s_ashr_i32 s22, s55, 31
	s_lshr_b32 s22, s22, 29
	s_add_i32 s23, s55, s22
	s_ashr_i32 s22, s23, 3
	s_lshl_b32 s54, s22, 2
	s_add_i32 s54, s54, 0
	s_add_i32 s54, s54, 0x25a04
	v_mov_b32_e32 v2, s54
	ds_read_b32 v2, v2
	s_and_b32 s23, s23, -8
	s_sub_i32 s58, s55, s23
	s_ashr_i32 s23, s22, 31
	s_lshl_b32 s94, s22, 8
	s_lshl_b32 s95, s58, 8
	s_lshl_b64 s[22:23], s[22:23], 19
	s_waitcnt lgkmcnt(0)
	v_readfirstlane_b32 s54, v2
	s_add_u32 s56, s30, s22
	s_addc_u32 s57, s31, s23
	s_ashr_i32 s55, s54, 31
	s_lshl_b64 s[22:23], s[54:55], 22
	v_readlane_b32 s55, v252, 3
	s_add_u32 s55, s55, s22
	s_addc_u32 s68, s84, s23
	s_ashr_i32 s59, s58, 31
	s_lshl_b64 s[22:23], s[58:59], 19
	s_add_u32 s58, s55, s22
	s_addc_u32 s59, s68, s23
